# gla_local/ssd_local state tiles: transposed MFMA output staged through per-wave LDS scratch and stored as full 16-byte lines (8 stores per wave instead of 64 two-byte stores); plus LN1 gain preload
# baseline (speedup 1.0000x reference)
.LBB0_287:
	s_or_b64 exec, exec, s[50:51]
	v_lshrrev_b32_e32 v128, 3, v2
	v_and_b32_e32 v4, 2, v128
	v_bfe_u32 v5, v2, 1, 1
	v_readlane_b32 s12, v253, 32
	v_lshrrev_b32_e32 v6, 4, v2
	v_and_b32_e32 v6, 2, v6
	v_or3_b32 v4, v4, v5, s12
	v_lshlrev_b32_e32 v5, 2, v105
	v_lshrrev_b32_e32 v3, 2, v2
	v_or_b32_e32 v7, v5, v6
	v_and_b32_e32 v107, 31, v2
	v_bitop3_b32 v5, v5, v4, v6 bitop3:0x36
	v_readlane_b32 s12, v253, 33
	v_lshlrev_b32_e32 v6, 3, v2
	v_bfe_u32 v129, v2, 5, 1
	v_lshlrev_b32_e32 v2, 8, v3
	v_bitop3_b32 v4, v7, v4, 1 bitop3:0x36
	v_lshl_add_u32 v5, v5, 4, s12
	v_and_b32_e32 v6, 8, v6
	v_and_b32_e32 v8, 0xb00, v2
	v_lshl_add_u32 v4, v4, 4, s12
	v_add3_u32 v131, v5, v6, v8
	v_add3_u32 v132, v4, v8, v6
	s_waitcnt lgkmcnt(0)
	s_barrier
	ds_read_b64_tr_b16 v[2:3], v131 offset:40960
	ds_read_b64_tr_b16 v[4:5], v132 offset:41984
	v_lshl_add_u32 v130, v107, 8, 0
	v_bitop3_b32 v6, v0, v129, v105 bitop3:0x36
	v_lshl_add_u32 v10, v6, 4, v130
	ds_read_b128 v[6:9], v10 offset:8192
	s_waitcnt lgkmcnt(0)
	v_mfma_f32_32x32x16_bf16 v[50:65], v[6:9], v[2:5], 0
	ds_read_b128 v[6:9], v10 offset:16384
	v_or_b32_e32 v124, 2, v129
	v_bitop3_b32 v124, v0, v124, v105 bitop3:0x36
	v_lshl_add_u32 v133, v124, 4, v130
	v_lshlrev_b64 v[108:109], 22, v[108:109]
	v_lshl_add_u64 v[108:109], s[6:7], 0, v[108:109]
	s_lshl_b32 s30, s53, 16
	s_waitcnt lgkmcnt(0)
	v_mfma_f32_32x32x16_bf16 v[34:49], v[6:9], v[2:5], 0
	ds_read_b128 v[6:9], v10 offset:24576
	v_lshl_add_u64 v[108:109], v[108:109], 0, s[30:31]
	s_andn2_b64 vcc, exec, s[48:49]
	s_waitcnt lgkmcnt(0)
	v_mfma_f32_32x32x16_bf16 v[18:33], v[6:9], v[2:5], 0
	ds_read_b128 v[6:9], v10 offset:32768
	ds_read_b64_tr_b16 v[120:121], v131 offset:45056
	ds_read_b64_tr_b16 v[122:123], v132 offset:46080
	ds_read_b128 v[124:127], v133 offset:8192
	s_waitcnt lgkmcnt(0)
	v_mfma_f32_32x32x16_bf16 v[50:65], v[124:127], v[120:123], v[50:65]
	ds_read_b128 v[124:127], v133 offset:16384
	s_waitcnt lgkmcnt(0)
	v_mfma_f32_32x32x16_bf16 v[34:49], v[124:127], v[120:123], v[34:49]
	ds_read_b128 v[124:127], v133 offset:24576
	v_mfma_f32_32x32x16_bf16 v[2:17], v[6:9], v[2:5], 0
	s_waitcnt lgkmcnt(0)
	v_mfma_f32_32x32x16_bf16 v[18:33], v[124:127], v[120:123], v[18:33]
	ds_read_b128 v[124:127], v133 offset:32768
	s_waitcnt lgkmcnt(0)
	v_mfma_f32_32x32x16_bf16 v[2:17], v[124:127], v[120:123], v[2:17]
	v_or_b32_e32 v124, 4, v129
	v_bitop3_b32 v124, v0, v124, v105 bitop3:0x36
	v_lshl_add_u32 v133, v124, 4, v130
	ds_read_b64_tr_b16 v[120:121], v131 offset:49152
	ds_read_b64_tr_b16 v[122:123], v132 offset:50176
	ds_read_b128 v[124:127], v133 offset:8192
	s_waitcnt lgkmcnt(0)
	v_mfma_f32_32x32x16_bf16 v[50:65], v[124:127], v[120:123], v[50:65]
	ds_read_b128 v[124:127], v133 offset:16384
	s_waitcnt lgkmcnt(0)
	v_mfma_f32_32x32x16_bf16 v[34:49], v[124:127], v[120:123], v[34:49]
	ds_read_b128 v[124:127], v133 offset:24576
	s_waitcnt lgkmcnt(0)
	v_mfma_f32_32x32x16_bf16 v[18:33], v[124:127], v[120:123], v[18:33]
	ds_read_b128 v[124:127], v133 offset:32768
	s_waitcnt lgkmcnt(0)
	v_mfma_f32_32x32x16_bf16 v[2:17], v[124:127], v[120:123], v[2:17]
	v_or_b32_e32 v124, 6, v129
	v_bitop3_b32 v0, v0, v124, v105 bitop3:0x36
	v_lshl_add_u32 v0, v0, 4, v130
	ds_read_b64_tr_b16 v[120:121], v131 offset:53248
	ds_read_b64_tr_b16 v[122:123], v132 offset:54272
	ds_read_b128 v[124:127], v0 offset:8192
	s_waitcnt lgkmcnt(0)
	v_mfma_f32_32x32x16_bf16 v[50:65], v[124:127], v[120:123], v[50:65]
	ds_read_b128 v[124:127], v0 offset:16384
	s_waitcnt lgkmcnt(0)
	v_mfma_f32_32x32x16_bf16 v[34:49], v[124:127], v[120:123], v[34:49]
	ds_read_b128 v[124:127], v0 offset:24576
	s_waitcnt lgkmcnt(0)
	v_mfma_f32_32x32x16_bf16 v[18:33], v[124:127], v[120:123], v[18:33]
	ds_read_b128 v[124:127], v0 offset:32768
	s_waitcnt lgkmcnt(0)
	v_mfma_f32_32x32x16_bf16 v[2:17], v[124:127], v[120:123], v[2:17]
	s_nop 7
	s_nop 3
	v_mov_b32_e32 v133, v128
	s_lshl_b32 s101, s90, 8
	s_add_i32 s100, s101, 0x16000
	v_and_b32_e32 v120, 3, v107
	v_lshlrev_b32_e32 v120, 6, v120
	v_bfe_u32 v123, v107, 2, 2
	v_lshl_or_b32 v120, v123, 4, v120
	v_lshlrev_b32_e32 v121, 8, v107
	v_and_b32_e32 v123, 4, v133
	v_lshl_add_u32 v121, v123, 1, v121
	v_add3_u32 v121, v121, v120, s100
	v_cvt_pk_bf16_f32 v128, v50, v51
	v_cvt_pk_bf16_f32 v129, v52, v53
	ds_write_b64 v121, v[128:129]
	v_cvt_pk_bf16_f32 v130, v54, v55
	v_cvt_pk_bf16_f32 v131, v56, v57
	v_xor_b32_e32 v123, 16, v121
	ds_write_b64 v123, v[130:131]
	v_cvt_pk_bf16_f32 v128, v58, v59
	v_cvt_pk_bf16_f32 v129, v60, v61
	v_xor_b32_e32 v123, 32, v121
	ds_write_b64 v123, v[128:129]
	v_cvt_pk_bf16_f32 v130, v62, v63
	v_cvt_pk_bf16_f32 v131, v64, v65
	v_xor_b32_e32 v123, 48, v121
	ds_write_b64 v123, v[130:131]
	v_cvt_pk_bf16_f32 v128, v34, v35
	v_cvt_pk_bf16_f32 v129, v36, v37
	v_xor_b32_e32 v123, 64, v121
	ds_write_b64 v123, v[128:129]
	v_cvt_pk_bf16_f32 v130, v38, v39
	v_cvt_pk_bf16_f32 v131, v40, v41
	v_xor_b32_e32 v123, 0x50, v121
	ds_write_b64 v123, v[130:131]
	v_cvt_pk_bf16_f32 v128, v42, v43
	v_cvt_pk_bf16_f32 v129, v44, v45
	v_xor_b32_e32 v123, 0x60, v121
	ds_write_b64 v123, v[128:129]
	v_cvt_pk_bf16_f32 v130, v46, v47
	v_cvt_pk_bf16_f32 v131, v48, v49
	v_xor_b32_e32 v123, 0x70, v121
	ds_write_b64 v123, v[130:131]
	v_cvt_pk_bf16_f32 v128, v18, v19
	v_cvt_pk_bf16_f32 v129, v20, v21
	v_xor_b32_e32 v123, 0x80, v121
	ds_write_b64 v123, v[128:129]
	v_cvt_pk_bf16_f32 v130, v22, v23
	v_cvt_pk_bf16_f32 v131, v24, v25
	v_xor_b32_e32 v123, 0x90, v121
	ds_write_b64 v123, v[130:131]
	v_cvt_pk_bf16_f32 v128, v26, v27
	v_cvt_pk_bf16_f32 v129, v28, v29
	v_xor_b32_e32 v123, 0xa0, v121
	ds_write_b64 v123, v[128:129]
	v_cvt_pk_bf16_f32 v130, v30, v31
	v_cvt_pk_bf16_f32 v131, v32, v33
	v_xor_b32_e32 v123, 0xb0, v121
	ds_write_b64 v123, v[130:131]
	v_cvt_pk_bf16_f32 v128, v2, v3
	v_cvt_pk_bf16_f32 v129, v4, v5
	v_xor_b32_e32 v123, 0xc0, v121
	ds_write_b64 v123, v[128:129]
	v_cvt_pk_bf16_f32 v130, v6, v7
	v_cvt_pk_bf16_f32 v131, v8, v9
	v_xor_b32_e32 v123, 0xd0, v121
	ds_write_b64 v123, v[130:131]
	v_cvt_pk_bf16_f32 v128, v10, v11
	v_cvt_pk_bf16_f32 v129, v12, v13
	v_xor_b32_e32 v123, 0xe0, v121
	ds_write_b64 v123, v[128:129]
	v_cvt_pk_bf16_f32 v130, v14, v15
	v_cvt_pk_bf16_f32 v131, v16, v17
	v_xor_b32_e32 v123, 0xf0, v121
	ds_write_b64 v123, v[130:131]
	v_and_b32_e32 v126, 15, v107
	v_bfe_u32 v127, v133, 1, 2
	v_lshlrev_b32_e32 v132, 2, v127
	v_xor_b32_e32 v132, v126, v132
	v_lshlrev_b32_e32 v127, 8, v127
	v_lshl_add_u32 v122, v132, 4, v127
	v_add_u32_e32 v122, s100, v122
	v_lshl_add_u32 v124, v126, 4, v127
	v_add_u32_e32 v124, s101, v124
	v_mov_b32_e32 v125, 0
	v_lshl_add_u64 v[108:109], v[108:109], 0, v[124:125]
	v_mov_b32_e32 v124, 0x1000
	v_lshl_add_u64 v[130:131], v[108:109], 0, v[124:125]
	s_waitcnt lgkmcnt(0)
	ds_read_b128 v[2:5], v122
	v_xor_b32_e32 v123, 16, v122
	ds_read_b128 v[6:9], v123 offset:1024
	v_xor_b32_e32 v123, 32, v122
	ds_read_b128 v[10:13], v123 offset:2048
	v_xor_b32_e32 v123, 48, v122
	ds_read_b128 v[14:17], v123 offset:3072
	ds_read_b128 v[18:21], v122 offset:4096
	v_xor_b32_e32 v123, 16, v122
	ds_read_b128 v[22:25], v123 offset:5120
	v_xor_b32_e32 v123, 32, v122
	ds_read_b128 v[26:29], v123 offset:6144
	v_xor_b32_e32 v123, 48, v122
	ds_read_b128 v[30:33], v123 offset:7168
	s_waitcnt lgkmcnt(7)
	global_store_dwordx4 v[108:109], v[2:5], off
	s_waitcnt lgkmcnt(6)
	global_store_dwordx4 v[108:109], v[6:9], off offset:1024
	s_waitcnt lgkmcnt(5)
	global_store_dwordx4 v[108:109], v[10:13], off offset:2048
	s_waitcnt lgkmcnt(4)
	global_store_dwordx4 v[108:109], v[14:17], off offset:3072
	s_waitcnt lgkmcnt(3)
	global_store_dwordx4 v[130:131], v[18:21], off
	s_waitcnt lgkmcnt(2)
	global_store_dwordx4 v[130:131], v[22:25], off offset:1024
	s_waitcnt lgkmcnt(1)
	global_store_dwordx4 v[130:131], v[26:29], off offset:2048
	s_waitcnt lgkmcnt(0)
	global_store_dwordx4 v[130:131], v[30:33], off offset:3072
	s_cbranch_vccz .LBB0_292

.LBB0_325:
	s_or_b64 exec, exec, s[40:41]
	v_mov_b32_e32 v0, v142
	s_waitcnt lgkmcnt(0)
	s_barrier
	v_readlane_b32 s18, v253, 35
	v_and_b32_e32 v156, 31, v0
	v_lshlrev_b32_e32 v3, 2, v0
	v_ashrrev_i32_e32 v157, 5, v0
	v_or_b32_e32 v2, s18, v156
	v_and_b32_e32 v158, 12, v3
	v_bfe_u32 v0, v0, 2, 2
	v_lshl_add_u32 v159, v2, 8, 0
	v_bitop3_b32 v2, v158, v157, v0 bitop3:0x36
	v_lshlrev_b32_e32 v6, 4, v2
	v_add_u32_e32 v2, v159, v6
	ds_read_b128 v[2:5], v2 offset:8192
	s_add_i32 s18, 0, 0x12000
	v_lshl_add_u32 v160, v156, 8, s18
	v_add_u32_e32 v10, v160, v6
	ds_read_b128 v[6:9], v10
	v_add_u32_e32 v148, 2, v157
	v_bitop3_b32 v148, v158, v148, v0 bitop3:0x36
	v_lshlrev_b32_e32 v152, 4, v148
	s_waitcnt lgkmcnt(0)
	v_mfma_f32_32x32x16_bf16 v[50:65], v[6:9], v[2:5], 0
	ds_read_b128 v[6:9], v10 offset:8192
	v_add_u32_e32 v148, v159, v152
	ds_read_b128 v[148:151], v148 offset:8192
	v_add_u32_e32 v161, v160, v152
	ds_read_b128 v[152:155], v161
	s_lshl_b64 s[20:21], s[48:49], 9
	v_readlane_b32 s18, v253, 47
	s_waitcnt lgkmcnt(2)
	v_mfma_f32_32x32x16_bf16 v[34:49], v[6:9], v[2:5], 0
	ds_read_b128 v[6:9], v10 offset:16384
	s_add_u32 s20, s20, s18
	s_addc_u32 s21, s21, 0
	v_lshl_add_u64 v[144:145], s[20:21], 0, v[144:145]
	v_lshl_add_u64 v[144:145], v[144:145], 0, v[146:147]
	v_readlane_b32 s18, v253, 34
	v_lshlrev_b64 v[144:145], 14, v[144:145]
	s_waitcnt lgkmcnt(0)
	v_mfma_f32_32x32x16_bf16 v[18:33], v[6:9], v[2:5], 0
	ds_read_b128 v[6:9], v10 offset:24576
	v_lshl_add_u32 v146, v157, 2, s18
	v_lshl_add_u64 v[144:145], s[6:7], 0, v[144:145]
	v_ashrrev_i32_e32 v147, 31, v146
	s_movk_i32 s18, 0x1000
	s_mov_b64 s[20:21], 0x1100
	s_mov_b32 s27, s12
	v_mfma_f32_32x32x16_bf16 v[50:65], v[152:155], v[148:151], v[50:65]
	ds_read_b128 v[152:155], v161 offset:8192
	s_waitcnt lgkmcnt(0)
	v_mfma_f32_32x32x16_bf16 v[34:49], v[152:155], v[148:151], v[34:49]
	ds_read_b128 v[152:155], v161 offset:16384
	v_mfma_f32_32x32x16_bf16 v[2:17], v[6:9], v[2:5], 0
	s_waitcnt lgkmcnt(0)
	v_mfma_f32_32x32x16_bf16 v[18:33], v[152:155], v[148:151], v[18:33]
	ds_read_b128 v[152:155], v161 offset:24576
	s_waitcnt lgkmcnt(0)
	v_mfma_f32_32x32x16_bf16 v[2:17], v[152:155], v[148:151], v[2:17]
	v_add_u32_e32 v148, 4, v157
	v_bitop3_b32 v148, v158, v148, v0 bitop3:0x36
	v_lshlrev_b32_e32 v152, 4, v148
	v_add_u32_e32 v148, v159, v152
	ds_read_b128 v[148:151], v148 offset:8192
	v_add_u32_e32 v161, v160, v152
	ds_read_b128 v[152:155], v161
	s_waitcnt lgkmcnt(0)
	v_mfma_f32_32x32x16_bf16 v[50:65], v[152:155], v[148:151], v[50:65]
	ds_read_b128 v[152:155], v161 offset:8192
	s_waitcnt lgkmcnt(0)
	v_mfma_f32_32x32x16_bf16 v[34:49], v[152:155], v[148:151], v[34:49]
	ds_read_b128 v[152:155], v161 offset:16384
	s_waitcnt lgkmcnt(0)
	v_mfma_f32_32x32x16_bf16 v[18:33], v[152:155], v[148:151], v[18:33]
	ds_read_b128 v[152:155], v161 offset:24576
	s_waitcnt lgkmcnt(0)
	v_mfma_f32_32x32x16_bf16 v[2:17], v[152:155], v[148:151], v[2:17]
	v_add_u32_e32 v148, 6, v157
	v_bitop3_b32 v148, v158, v148, v0 bitop3:0x36
	v_lshlrev_b32_e32 v152, 4, v148
	v_add_u32_e32 v148, v159, v152
	ds_read_b128 v[148:151], v148 offset:8192
	v_add_u32_e32 v161, v160, v152
	ds_read_b128 v[152:155], v161
	s_waitcnt lgkmcnt(0)
	v_mfma_f32_32x32x16_bf16 v[50:65], v[152:155], v[148:151], v[50:65]
	ds_read_b128 v[152:155], v161 offset:8192
	s_waitcnt lgkmcnt(0)
	v_mfma_f32_32x32x16_bf16 v[34:49], v[152:155], v[148:151], v[34:49]
	ds_read_b128 v[152:155], v161 offset:16384
	s_waitcnt lgkmcnt(0)
	v_mfma_f32_32x32x16_bf16 v[18:33], v[152:155], v[148:151], v[18:33]
	ds_read_b128 v[152:155], v161 offset:24576
	s_waitcnt lgkmcnt(0)
	v_mfma_f32_32x32x16_bf16 v[2:17], v[152:155], v[148:151], v[2:17]
	v_add_u32_e32 v148, 8, v157
	v_bitop3_b32 v148, v158, v148, v0 bitop3:0x36
	v_lshlrev_b32_e32 v152, 4, v148
	v_add_u32_e32 v148, v159, v152
	ds_read_b128 v[148:151], v148 offset:8192
	v_add_u32_e32 v161, v160, v152
	ds_read_b128 v[152:155], v161
	s_waitcnt lgkmcnt(0)
	v_mfma_f32_32x32x16_bf16 v[50:65], v[152:155], v[148:151], v[50:65]
	ds_read_b128 v[152:155], v161 offset:8192
	s_waitcnt lgkmcnt(0)
	v_mfma_f32_32x32x16_bf16 v[34:49], v[152:155], v[148:151], v[34:49]
	ds_read_b128 v[152:155], v161 offset:16384
	s_waitcnt lgkmcnt(0)
	v_mfma_f32_32x32x16_bf16 v[18:33], v[152:155], v[148:151], v[18:33]
	ds_read_b128 v[152:155], v161 offset:24576
	s_waitcnt lgkmcnt(0)
	v_mfma_f32_32x32x16_bf16 v[2:17], v[152:155], v[148:151], v[2:17]
	v_add_u32_e32 v148, 10, v157
	v_bitop3_b32 v148, v158, v148, v0 bitop3:0x36
	v_lshlrev_b32_e32 v152, 4, v148
	v_add_u32_e32 v148, v159, v152
	ds_read_b128 v[148:151], v148 offset:8192
	v_add_u32_e32 v161, v160, v152
	ds_read_b128 v[152:155], v161
	s_waitcnt lgkmcnt(0)
	v_mfma_f32_32x32x16_bf16 v[50:65], v[152:155], v[148:151], v[50:65]
	ds_read_b128 v[152:155], v161 offset:8192
	s_waitcnt lgkmcnt(0)
	v_mfma_f32_32x32x16_bf16 v[34:49], v[152:155], v[148:151], v[34:49]
	ds_read_b128 v[152:155], v161 offset:16384
	s_waitcnt lgkmcnt(0)
	v_mfma_f32_32x32x16_bf16 v[18:33], v[152:155], v[148:151], v[18:33]
	ds_read_b128 v[152:155], v161 offset:24576
	s_waitcnt lgkmcnt(0)
	v_mfma_f32_32x32x16_bf16 v[2:17], v[152:155], v[148:151], v[2:17]
	v_add_u32_e32 v148, 12, v157
	v_bitop3_b32 v148, v158, v148, v0 bitop3:0x36
	v_lshlrev_b32_e32 v152, 4, v148
	v_add_u32_e32 v148, v159, v152
	ds_read_b128 v[148:151], v148 offset:8192
	v_add_u32_e32 v161, v160, v152
	ds_read_b128 v[152:155], v161
	s_waitcnt lgkmcnt(0)
	v_mfma_f32_32x32x16_bf16 v[50:65], v[152:155], v[148:151], v[50:65]
	ds_read_b128 v[152:155], v161 offset:8192
	s_waitcnt lgkmcnt(0)
	v_mfma_f32_32x32x16_bf16 v[34:49], v[152:155], v[148:151], v[34:49]
	ds_read_b128 v[152:155], v161 offset:16384
	s_waitcnt lgkmcnt(0)
	v_mfma_f32_32x32x16_bf16 v[18:33], v[152:155], v[148:151], v[18:33]
	ds_read_b128 v[152:155], v161 offset:24576
	s_waitcnt lgkmcnt(0)
	v_mfma_f32_32x32x16_bf16 v[2:17], v[152:155], v[148:151], v[2:17]
	v_add_u32_e32 v148, 14, v157
	v_bitop3_b32 v0, v158, v148, v0 bitop3:0x36
	v_lshlrev_b32_e32 v0, 4, v0
	v_add_u32_e32 v148, v159, v0
	ds_read_b128 v[148:151], v148 offset:8192
	v_add_u32_e32 v0, v160, v0
	ds_read_b128 v[152:155], v0
	s_waitcnt lgkmcnt(0)
	v_mfma_f32_32x32x16_bf16 v[50:65], v[152:155], v[148:151], v[50:65]
	ds_read_b128 v[152:155], v0 offset:8192
	s_waitcnt lgkmcnt(0)
	v_mfma_f32_32x32x16_bf16 v[34:49], v[152:155], v[148:151], v[34:49]
	ds_read_b128 v[152:155], v0 offset:16384
	s_waitcnt lgkmcnt(0)
	v_mfma_f32_32x32x16_bf16 v[18:33], v[152:155], v[148:151], v[18:33]
	ds_read_b128 v[152:155], v0 offset:24576
	s_waitcnt lgkmcnt(0)
	v_mfma_f32_32x32x16_bf16 v[2:17], v[152:155], v[148:151], v[2:17]
	s_barrier
	v_lshrrev_b32_e32 v146, 3, v142
	s_nop 3
	s_lshl_b32 s101, s90, 8
	s_add_i32 s100, s101, 0x2000
	s_and_b32 s18, s101, 0x2000
	v_and_b32_e32 v148, 3, v156
	v_lshlrev_b32_e32 v148, 6, v148
	v_bfe_u32 v151, v156, 2, 2
	v_lshl_or_b32 v148, v151, 4, v148
	v_lshlrev_b32_e32 v149, 8, v156
	v_and_b32_e32 v151, 4, v146
	v_lshl_add_u32 v149, v151, 1, v149
	v_add3_u32 v149, v149, v148, s100
	v_cvt_pk_bf16_f32 v158, v50, v51
	v_cvt_pk_bf16_f32 v159, v52, v53
	ds_write_b64 v149, v[158:159]
	v_cvt_pk_bf16_f32 v160, v54, v55
	v_cvt_pk_bf16_f32 v161, v56, v57
	v_xor_b32_e32 v151, 16, v149
	ds_write_b64 v151, v[160:161]
	v_cvt_pk_bf16_f32 v158, v58, v59
	v_cvt_pk_bf16_f32 v159, v60, v61
	v_xor_b32_e32 v151, 32, v149
	ds_write_b64 v151, v[158:159]
	v_cvt_pk_bf16_f32 v160, v62, v63
	v_cvt_pk_bf16_f32 v161, v64, v65
	v_xor_b32_e32 v151, 48, v149
	ds_write_b64 v151, v[160:161]
	v_cvt_pk_bf16_f32 v158, v34, v35
	v_cvt_pk_bf16_f32 v159, v36, v37
	v_xor_b32_e32 v151, 64, v149
	ds_write_b64 v151, v[158:159]
	v_cvt_pk_bf16_f32 v160, v38, v39
	v_cvt_pk_bf16_f32 v161, v40, v41
	v_xor_b32_e32 v151, 0x50, v149
	ds_write_b64 v151, v[160:161]
	v_cvt_pk_bf16_f32 v158, v42, v43
	v_cvt_pk_bf16_f32 v159, v44, v45
	v_xor_b32_e32 v151, 0x60, v149
	ds_write_b64 v151, v[158:159]
	v_cvt_pk_bf16_f32 v160, v46, v47
	v_cvt_pk_bf16_f32 v161, v48, v49
	v_xor_b32_e32 v151, 0x70, v149
	ds_write_b64 v151, v[160:161]
	v_cvt_pk_bf16_f32 v158, v18, v19
	v_cvt_pk_bf16_f32 v159, v20, v21
	v_xor_b32_e32 v151, 0x80, v149
	ds_write_b64 v151, v[158:159]
	v_cvt_pk_bf16_f32 v160, v22, v23
	v_cvt_pk_bf16_f32 v161, v24, v25
	v_xor_b32_e32 v151, 0x90, v149
	ds_write_b64 v151, v[160:161]
	v_cvt_pk_bf16_f32 v158, v26, v27
	v_cvt_pk_bf16_f32 v159, v28, v29
	v_xor_b32_e32 v151, 0xa0, v149
	ds_write_b64 v151, v[158:159]
	v_cvt_pk_bf16_f32 v160, v30, v31
	v_cvt_pk_bf16_f32 v161, v32, v33
	v_xor_b32_e32 v151, 0xb0, v149
	ds_write_b64 v151, v[160:161]
	v_cvt_pk_bf16_f32 v158, v2, v3
	v_cvt_pk_bf16_f32 v159, v4, v5
	v_xor_b32_e32 v151, 0xc0, v149
	ds_write_b64 v151, v[158:159]
	v_cvt_pk_bf16_f32 v160, v6, v7
	v_cvt_pk_bf16_f32 v161, v8, v9
	v_xor_b32_e32 v151, 0xd0, v149
	ds_write_b64 v151, v[160:161]
	v_cvt_pk_bf16_f32 v158, v10, v11
	v_cvt_pk_bf16_f32 v159, v12, v13
	v_xor_b32_e32 v151, 0xe0, v149
	ds_write_b64 v151, v[158:159]
	v_cvt_pk_bf16_f32 v160, v14, v15
	v_cvt_pk_bf16_f32 v161, v16, v17
	v_xor_b32_e32 v151, 0xf0, v149
	ds_write_b64 v151, v[160:161]
	v_and_b32_e32 v154, 15, v156
	v_bfe_u32 v155, v146, 1, 2
	v_lshlrev_b32_e32 v157, 2, v155
	v_xor_b32_e32 v157, v154, v157
	v_lshlrev_b32_e32 v155, 8, v155
	v_lshl_add_u32 v150, v157, 4, v155
	v_add_u32_e32 v150, s100, v150
	v_lshl_add_u32 v152, v154, 4, v155
	v_add_u32_e32 v152, s18, v152
	v_mov_b32_e32 v153, 0
	v_lshl_add_u64 v[144:145], v[144:145], 0, v[152:153]
	v_mov_b32_e32 v152, 0x1000
	v_lshl_add_u64 v[160:161], v[144:145], 0, v[152:153]
	s_waitcnt lgkmcnt(0)
	ds_read_b128 v[2:5], v150
	v_xor_b32_e32 v151, 16, v150
	ds_read_b128 v[6:9], v151 offset:1024
	v_xor_b32_e32 v151, 32, v150
	ds_read_b128 v[10:13], v151 offset:2048
	v_xor_b32_e32 v151, 48, v150
	ds_read_b128 v[14:17], v151 offset:3072
	ds_read_b128 v[18:21], v150 offset:4096
	v_xor_b32_e32 v151, 16, v150
	ds_read_b128 v[22:25], v151 offset:5120
	v_xor_b32_e32 v151, 32, v150
	ds_read_b128 v[26:29], v151 offset:6144
	v_xor_b32_e32 v151, 48, v150
	ds_read_b128 v[30:33], v151 offset:7168
	s_waitcnt lgkmcnt(7)
	global_store_dwordx4 v[144:145], v[2:5], off
	s_waitcnt lgkmcnt(6)
	global_store_dwordx4 v[144:145], v[6:9], off offset:1024
	s_waitcnt lgkmcnt(5)
	global_store_dwordx4 v[144:145], v[10:13], off offset:2048
	s_waitcnt lgkmcnt(4)
	global_store_dwordx4 v[144:145], v[14:17], off offset:3072
	s_waitcnt lgkmcnt(3)
	global_store_dwordx4 v[160:161], v[18:21], off
	s_waitcnt lgkmcnt(2)
	global_store_dwordx4 v[160:161], v[22:25], off offset:1024
	s_waitcnt lgkmcnt(1)
	global_store_dwordx4 v[160:161], v[26:29], off offset:2048
	s_waitcnt lgkmcnt(0)
	global_store_dwordx4 v[160:161], v[30:33], off offset:3072
	s_andn2_b64 vcc, exec, s[46:47]
	s_cbranch_vccz .LBB0_402
